# k_point: Wk1/Wk2 LDS images re-laid out with 144-B row stride (was 160) so the row-major rowproj ds_read2_b64 fragment reads are bank-conflict-free
# speedup vs baseline: 1.0418x; 1.0251x over previous
.LBB0_20:
	s_or_b64 exec, exec, s[4:5]
	s_waitcnt vmcnt(5)
	v_cvt_pk_f16_f32 v1, v24, v25
	v_cvt_pk_f16_f32 v0, v22, v23
	v_lshlrev_b32_e32 v135, 3, v106
	ds_write_b64 v135, v[0:1] offset:37888
	s_waitcnt vmcnt(4)
	v_cvt_pk_f16_f32 v1, v20, v21
	v_cvt_pk_f16_f32 v0, v18, v19
	ds_write_b64 v135, v[0:1] offset:41984
	s_and_saveexec_b64 s[4:5], s[2:3]
	s_cbranch_execz .LBB0_22
	v_mul_u32_u24_e32 v18, 0xe39, v106
	s_movk_i32 s6, 0xffee
	v_mul_i32_i24_sdwa v19, v18, s6 dst_sel:DWORD dst_unused:UNUSED_PAD src0_sel:WORD_1 src1_sel:DWORD
	s_movk_i32 s6, 0xa0
	s_waitcnt vmcnt(3)
	v_cvt_pk_f16_f32 v0, v14, v15
	v_mul_u32_u24_sdwa v14, v18, s6 dst_sel:DWORD dst_unused:UNUSED_PAD src0_sel:WORD_1 src1_sel:DWORD
	v_add_lshl_u32 v15, v19, v106, 3
	v_cvt_pk_f16_f32 v1, v16, v17
	v_add3_u32 v14, 0, v14, v15
	ds_write_b64 v135, v[0:1] offset:46080
.LBB0_22:
	s_or_b64 exec, exec, s[4:5]
	s_waitcnt vmcnt(2)
	v_cvt_pk_f16_f32 v1, v12, v13
	v_cvt_pk_f16_f32 v0, v10, v11
	ds_write_b64 v135, v[0:1] offset:49408
	s_waitcnt vmcnt(1)
	v_cvt_pk_f16_f32 v1, v8, v9
	v_cvt_pk_f16_f32 v0, v6, v7
	ds_write_b64 v135, v[0:1] offset:53504
	s_and_saveexec_b64 s[0:1], s[2:3]
	s_cbranch_execz .LBB0_24
	v_mul_u32_u24_e32 v6, 0xe39, v106
	s_movk_i32 s2, 0xffee
	v_mul_i32_i24_sdwa v7, v6, s2 dst_sel:DWORD dst_unused:UNUSED_PAD src0_sel:WORD_1 src1_sel:DWORD
	s_movk_i32 s2, 0xa0
	s_waitcnt vmcnt(0)
	v_cvt_pk_f16_f32 v0, v2, v3
	v_mul_u32_u24_sdwa v2, v6, s2 dst_sel:DWORD dst_unused:UNUSED_PAD src0_sel:WORD_1 src1_sel:DWORD
	v_add_lshl_u32 v3, v7, v106, 3
	v_cvt_pk_f16_f32 v1, v4, v5
	v_add3_u32 v2, 0, v2, v3
	ds_write_b64 v135, v[0:1] offset:57600

.LBB0_26:
	s_or_b64 exec, exec, s[2:3]
	v_or_b32_e32 v0, 2, v104
	s_movk_i32 s0, 0x2d00
	v_mad_u32_u24 v28, v0, s0, 0
	v_mul_u32_u24_e32 v0, 0x140, v0
	v_lshlrev_b32_e32 v1, 2, v93
	v_add_u32_e32 v30, v28, v88
	v_add3_u32 v29, s11, v0, v1
	v_add3_u32 v32, v28, v92, v88
	v_add_u32_e32 v33, v30, v92
	s_waitcnt vmcnt(0)
	ds_read_b128 v[0:3], v29
	ds_read_b64_tr_b16 v[4:5], v32
	ds_read_b64_tr_b16 v[6:7], v33 offset:2560
	v_mov_b32_e32 v62, v52
	ds_read_b64_tr_b16 v[8:9], v32 offset:32
	v_lshl_add_u32 v31, v91, 1, v28
	s_waitcnt lgkmcnt(1)
	v_mfma_f32_16x16x32_f16 v[4:7], v[4:7], v[62:65], v[0:3]
	ds_read_b64_tr_b16 v[10:11], v33 offset:2592
	ds_read_b64_tr_b16 v[12:13], v32 offset:5120
	ds_read_b64_tr_b16 v[14:15], v33 offset:7680
	v_add_u32_e32 v34, v31, v92
	ds_read_b64_tr_b16 v[0:1], v34 offset:10240
	v_mov_b32_e32 v2, 0
	v_mov_b32_e32 v3, v2
	s_waitcnt lgkmcnt(1)
	v_mfma_f32_16x16x32_f16 v[4:7], v[12:15], v[58:61], v[4:7]
	ds_read_b64_tr_b16 v[12:13], v34 offset:10272
	ds_read_b128 v[16:19], v29 offset:64
	v_mov_b32_e32 v14, v2
	s_waitcnt lgkmcnt(2)
	v_mfma_f32_16x16x32_f16 v[4:7], v[0:3], v[54:57], v[4:7]
	ds_read_b64_tr_b16 v[20:21], v32 offset:5152
	ds_read_b64_tr_b16 v[22:23], v33 offset:7712
	v_mov_b32_e32 v15, v2
	s_waitcnt lgkmcnt(2)
	v_mfma_f32_16x16x32_f16 v[8:11], v[8:11], v[62:65], v[16:19]
	ds_read_b64_tr_b16 v[24:25], v32 offset:64
	v_add3_u32 v28, v28, v95, v88
	v_add_u32_e32 v30, v30, v95
	ds_read_b128 v[16:19], v29 offset:128
	s_waitcnt lgkmcnt(2)
	v_mfma_f32_16x16x32_f16 v[8:11], v[20:23], v[58:61], v[8:11]
	ds_read_b64_tr_b16 v[26:27], v33 offset:2624
	ds_read_b64_tr_b16 v[20:21], v32 offset:5184
	s_movk_i32 s2, 0x90
	v_mfma_f32_16x16x32_f16 v[8:11], v[12:15], v[54:57], v[8:11]
	ds_read_b64_tr_b16 v[22:23], v33 offset:7744
	ds_read_b64_tr_b16 v[0:1], v34 offset:10304
	v_mad_u32_u24 v35, v102, s2, v86
	s_waitcnt lgkmcnt(3)
	v_mfma_f32_16x16x32_f16 v[12:15], v[24:27], v[62:65], v[16:19]
	ds_read_b64_tr_b16 v[24:25], v28
	s_nop 1
	ds_read_b128 v[16:19], v29 offset:192
	v_add_u32_e32 v49, v35, v50
	s_waitcnt lgkmcnt(3)
	v_mfma_f32_16x16x32_f16 v[12:15], v[20:23], v[58:61], v[12:15]
	ds_read_b64_tr_b16 v[26:27], v30 offset:2560
	ds_read_b64_tr_b16 v[20:21], v28 offset:5120
	v_lshlrev_b32_e32 v48, 1, v87
	s_waitcnt lgkmcnt(4)
	v_mfma_f32_16x16x32_f16 v[12:15], v[0:3], v[54:57], v[12:15]
	ds_read_b64_tr_b16 v[22:23], v30 offset:7680
	v_add_u32_e32 v0, v31, v95
	ds_read_b64_tr_b16 v[0:1], v0 offset:10240
	s_waitcnt lgkmcnt(3)
	v_mfma_f32_16x16x32_f16 v[16:19], v[24:27], v[62:65], v[16:19]
	ds_read_b128 v[24:27], v29 offset:256
	ds_read_b64_tr_b16 v[28:29], v32 offset:128
	v_add_u32_e32 v36, v35, v48
	s_waitcnt lgkmcnt(3)
	v_mfma_f32_16x16x32_f16 v[16:19], v[20:23], v[58:61], v[16:19]
	ds_read_b64_tr_b16 v[30:31], v33 offset:2688
	ds_read_b64_tr_b16 v[20:21], v32 offset:5248
	v_add_u32_e32 v32, 0xb000, v49
	s_waitcnt lgkmcnt(4)
	v_mfma_f32_16x16x32_f16 v[16:19], v[0:3], v[54:57], v[16:19]
	ds_read_b64_tr_b16 v[22:23], v33 offset:7808
	ds_read_b64_tr_b16 v[0:1], v34 offset:10368
	v_add_u32_e32 v44, 0x80, v36
	v_add_u32_e32 v134, 0x180, v36
	s_waitcnt lgkmcnt(3)
	v_mfma_f32_16x16x32_f16 v[24:27], v[28:31], v[62:65], v[24:27]
	ds_read2_b64 v[28:31], v32 offset0:128 offset1:132
	ds_read2_b64 v[32:35], v32 offset0:136 offset1:140
	v_add_u32_e32 v40, 0xb800, v49
	s_waitcnt lgkmcnt(3)
	v_mfma_f32_16x16x32_f16 v[20:23], v[20:23], v[58:61], v[24:27]
	ds_read2_b64 v[36:39], v40 offset0:160 offset1:164
	v_cmp_gt_u32_e64 s[0:1], 32, v103
	v_cvt_pk_f16_f32 v11, v10, v11
	ds_read2st64_b64 v[126:129], v44 offset0:90 offset1:99
	s_waitcnt lgkmcnt(4)
	v_mfma_f32_16x16x32_f16 v[20:23], v[0:3], v[54:57], v[20:23]
	v_cvt_pk_f16_f32 v10, v8, v9
	v_cvt_pk_f16_f32 v9, v6, v7
	v_cvt_pk_f16_f32 v8, v4, v5
	ds_read2_b64 v[4:7], v40 offset0:168 offset1:172
	v_cvt_pk_f16_f32 v19, v18, v19
	s_nop 2
	v_cvt_pk_f16_f32 v0, v22, v23
	v_cvt_pk_f16_f32 v1, v20, v21
	v_cndmask_b32_e64 v21, 0, v0, s[0:1]
	v_add_u32_e32 v0, 0xc600, v49
	ds_read2_b64 v[40:43], v0 offset1:4
	s_waitcnt lgkmcnt(5)
	v_mfma_f32_16x16x32_f16 v[28:31], v[28:31], v[8:11], 0
	v_cndmask_b32_e64 v20, 0, v1, s[0:1]
	v_cvt_pk_f16_f32 v18, v16, v17
	v_cvt_pk_f16_f32 v17, v14, v15
	v_cvt_pk_f16_f32 v16, v12, v13
	ds_read2_b64 v[12:15], v0 offset0:8 offset1:12
	s_waitcnt lgkmcnt(3)
	v_mov_b32_e32 v0, v126
	v_mov_b32_e32 v1, v127
	ds_read2st64_b64 v[130:133], v134 offset0:94 offset1:103
	v_mfma_f32_16x16x32_f16 v[28:31], v[32:35], v[16:19], v[28:31]
	v_mov_b32_e32 v22, v2
	v_mov_b32_e32 v23, v2
	v_add_u32_e32 v24, 0xce00, v49
	ds_read2_b64 v[32:35], v24 offset0:32 offset1:36
	ds_read2_b64 v[52:55], v24 offset0:40 offset1:44
	v_mfma_f32_16x16x32_f16 v[28:31], v[0:3], v[20:23], v[28:31]
	v_or_b32_e32 v0, 64, v102
	v_min_u32_e32 v0, 0x47, v0
	v_mad_u32_u24 v49, v0, s2, v86
	v_add_u32_e32 v0, v49, v50
	v_add_u32_e32 v0, 0xb000, v0
	ds_read2_b64 v[56:59], v0 offset0:128 offset1:132
	ds_read2_b64 v[60:63], v0 offset0:136 offset1:140
	v_mfma_f32_16x16x32_f16 v[36:39], v[36:39], v[8:11], 0
	s_waitcnt lgkmcnt(4)
	v_mov_b32_e32 v0, v130
	v_mov_b32_e32 v1, v131
	s_movk_i32 s2, 0x48
	s_waitcnt lgkmcnt(7)
	v_mfma_f32_16x16x32_f16 v[4:7], v[4:7], v[16:19], v[36:39]
	v_mov_b32_e32 v51, v2
	v_mfma_f32_16x16x32_f16 v[24:27], v[0:3], v[20:23], v[4:7]
	s_waitcnt lgkmcnt(4)
	v_mov_b32_e32 v0, v128
	v_mov_b32_e32 v1, v129
	v_mfma_f32_16x16x32_f16 v[4:7], v[40:43], v[8:11], 0
	v_mfma_f32_16x16x32_f16 v[4:7], v[12:15], v[16:19], v[4:7]
	v_mfma_f32_16x16x32_f16 v[12:15], v[0:3], v[20:23], v[4:7]
	v_mov_b32_e32 v0, v132
	v_mov_b32_e32 v1, v133
	s_waitcnt lgkmcnt(3)
	v_mfma_f32_16x16x32_f16 v[4:7], v[32:35], v[8:11], 0
	s_waitcnt lgkmcnt(2)
	v_mfma_f32_16x16x32_f16 v[4:7], v[52:55], v[16:19], v[4:7]
	v_mfma_f32_16x16x32_f16 v[32:35], v[0:3], v[20:23], v[4:7]
	v_add_u32_e32 v0, v49, v48
	ds_read_b64 v[0:1], v0 offset:46208
	s_waitcnt lgkmcnt(2)
	v_mfma_f32_16x16x32_f16 v[4:7], v[56:59], v[8:11], 0
	v_mul_lo_u32 v8, v97, s2
	s_mov_b32 s2, 0x3e2e1a92
	v_ashrrev_i32_e32 v9, 31, v8
	s_waitcnt lgkmcnt(1)
	v_mfma_f32_16x16x32_f16 v[4:7], v[60:63], v[16:19], v[4:7]
	s_waitcnt lgkmcnt(0)
	v_mfma_f32_16x16x32_f16 v[4:7], v[0:3], v[20:23], v[4:7]
	v_mov_b32_e32 v0, s63
	v_mov_b32_e32 v1, s61
	v_cndmask_b32_e32 v1, v0, v1, vcc
	v_mov_b32_e32 v0, s62
	v_mov_b32_e32 v3, s60
	v_cndmask_b32_e32 v0, v0, v3, vcc
	v_mov_b32_e32 v2, v29
	v_mov_b32_e32 v3, v30
	v_pk_mul_f32 v[2:3], v[2:3], s[2:3] op_sel_hi:[1,0]
	v_lshl_add_u64 v[0:1], v[8:9], 1, v[0:1]
	v_fma_mixlo_f16 v8, v28, s2, 0
	v_cvt_pk_f16_f32 v3, v2, v3
	v_pack_b32_f16 v2, v8, v3
	v_fma_mixlo_f16 v8, v31, s2, 0
	v_lshl_add_u64 v[0:1], v[0:1], 0, v[50:51]
	v_alignbit_b32 v3, v8, v3, 16
	global_store_dwordx2 v[0:1], v[2:3], off
	v_mov_b32_e32 v2, v25
	v_mov_b32_e32 v3, v26
	v_pk_mul_f32 v[2:3], v[2:3], s[2:3] op_sel_hi:[1,0]
	v_fma_mixlo_f16 v8, v24, s2, 0
	v_cvt_pk_f16_f32 v3, v2, v3
	v_pack_b32_f16 v2, v8, v3
	v_fma_mixlo_f16 v8, v27, s2, 0
	v_alignbit_b32 v3, v8, v3, 16
	global_store_dwordx2 v[0:1], v[2:3], off offset:32
	v_mov_b32_e32 v2, v13
	v_mov_b32_e32 v3, v14
	v_pk_mul_f32 v[2:3], v[2:3], s[2:3] op_sel_hi:[1,0]
	v_fma_mixlo_f16 v8, v12, s2, 0
	v_cvt_pk_f16_f32 v3, v2, v3
	v_pack_b32_f16 v2, v8, v3
	v_fma_mixlo_f16 v8, v15, s2, 0
	v_alignbit_b32 v3, v8, v3, 16
	global_store_dwordx2 v[0:1], v[2:3], off offset:64
	v_mov_b32_e32 v2, v33
	v_mov_b32_e32 v3, v34
	v_pk_mul_f32 v[2:3], v[2:3], s[2:3] op_sel_hi:[1,0]
	v_fma_mixlo_f16 v8, v32, s2, 0
	v_cvt_pk_f16_f32 v3, v2, v3
	v_pack_b32_f16 v2, v8, v3
	v_fma_mixlo_f16 v8, v35, s2, 0
	v_alignbit_b32 v3, v8, v3, 16
	global_store_dwordx2 v[0:1], v[2:3], off offset:96
	s_and_saveexec_b64 s[4:5], s[0:1]
	s_cbranch_execz .LBB0_28
	v_mov_b32_e32 v2, v5
	v_mov_b32_e32 v3, v6
	v_pk_mul_f32 v[2:3], v[2:3], s[2:3] op_sel_hi:[1,0]
	v_fma_mixlo_f16 v4, v4, s2, 0
	v_cvt_pk_f16_f32 v3, v2, v3
	v_pack_b32_f16 v2, v4, v3
	v_fma_mixlo_f16 v4, v7, s2, 0
	v_alignbit_b32 v3, v4, v3, 16
	global_store_dwordx2 v[0:1], v[2:3], off offset:128
